# MoBA/DSA attention loops, first half-step: waves 4-7 run finishSM(t) before bias-init+QK^T(t+1) (blocks proven register-independent) so MFMA and VALU of the two waves on a SIMD overlap
# speedup vs baseline: 1.0184x; 1.0026x over previous
_Z8mega_fwd4Args:
	v_readfirstlane_b32 s7, v0
	s_bfe_u32 s7, s7, 0x10008
	v_writelane_b32 v255, s7, 63
	s_load_dword s3, s[0:1], 0xc0
	s_add_u32 s4, s0, 0xc0
	v_writelane_b32 v254, s0, 0
	s_addc_u32 s5, s1, 0
	s_nop 0
	v_writelane_b32 v254, s1, 1
	v_writelane_b32 v254, s4, 2
	s_waitcnt lgkmcnt(0)
	s_and_b32 s0, s3, 7
	s_cmp_lg_u32 s0, 0
	v_writelane_b32 v254, s5, 3
	v_writelane_b32 v254, s3, 4
	v_writelane_b32 v254, s2, 5
	v_writelane_b32 v254, s2, 6
	s_cbranch_scc1 .LBB0_2
	v_readlane_b32 s3, v254, 5
	s_ashr_i32 s1, s3, 31
	s_lshr_b32 s1, s1, 29
	s_add_i32 s1, s3, s1
	v_readlane_b32 s0, v254, 4
	s_ashr_i32 s2, s1, 3
	s_and_b32 s1, s1, -8
	s_ashr_i32 s0, s0, 3
	s_sub_i32 s1, s3, s1
	s_mul_i32 s0, s0, s1
	s_add_i32 s0, s0, s2
	v_writelane_b32 v254, s0, 6

.LBB0_1143:
	v_readlane_b32 vcc_lo, v255, 63
	s_bitcmp1_b32 vcc_lo, 0
	s_cbranch_scc1 .Lsw1_B
.Lsw1_A:
	v_add_u32_e32 v66, 64, v216
	v_cvt_f32_i32_e32 v67, v66
	s_waitcnt vmcnt(0)
	v_lshrrev_b32_e32 v83, v208, v196
	v_and_b32_e32 v66, 1, v83
	v_cmp_eq_u32_e32 vcc, 1, v66
	v_mul_f32_e64 v82, -v178, v67
	v_fma_f32 v68, 0, v178, v82
	v_cndmask_b32_e32 v66, v243, v68, vcc
	v_and_b32_e32 v68, 2, v83
	v_fma_f32 v67, -v178, v67, v178
	v_cmp_ne_u32_e32 vcc, 0, v68
	v_and_b32_e32 v70, 8, v83
	v_pk_fma_f32 v[68:69], v[188:189], s[60:61], v[82:83] op_sel_hi:[1,1,0]
	v_cndmask_b32_e32 v67, v243, v67, vcc
	v_and_b32_e32 v71, 4, v83
	v_cmp_ne_u32_e32 vcc, 0, v70
	v_and_b32_e32 v72, 0x200, v83
	v_and_b32_e32 v73, 0x100, v83
	v_cndmask_b32_e32 v69, v243, v69, vcc
	v_cmp_ne_u32_e32 vcc, 0, v71
	v_pk_fma_f32 v[70:71], v[188:189], s[74:75], v[82:83] op_sel_hi:[1,1,0]
	v_and_b32_e32 v74, 0x800, v83
	v_cndmask_b32_e32 v68, v243, v68, vcc
	v_cmp_ne_u32_e32 vcc, 0, v72
	v_and_b32_e32 v75, 0x400, v83
	v_and_b32_e32 v76, 0x20000, v83
	v_cndmask_b32_e32 v71, v243, v71, vcc
	v_cmp_ne_u32_e32 vcc, 0, v73
	v_pk_fma_f32 v[72:73], v[188:189], s[62:63], v[82:83] op_sel_hi:[1,1,0]
	v_and_b32_e32 v77, 0x10000, v83
	v_cndmask_b32_e32 v70, v243, v70, vcc
	v_cmp_ne_u32_e32 vcc, 0, v74
	s_mov_b32 s2, 0x41900000
	s_mov_b32 s3, 0x41980000
	v_cndmask_b32_e32 v73, v243, v73, vcc
	v_cmp_ne_u32_e32 vcc, 0, v75
	v_pk_fma_f32 v[74:75], v[188:189], s[58:59], v[82:83] op_sel_hi:[1,1,0]
	v_and_b32_e32 v78, 0x80000, v83
	v_cndmask_b32_e32 v72, v243, v72, vcc
	v_cmp_ne_u32_e32 vcc, 0, v76
	v_and_b32_e32 v79, 0x40000, v83
	v_and_b32_e32 v80, 0x2000000, v83
	v_cndmask_b32_e32 v75, v243, v75, vcc
	v_cmp_ne_u32_e32 vcc, 0, v77
	v_pk_fma_f32 v[76:77], v[188:189], s[2:3], v[82:83] op_sel_hi:[1,1,0]
	s_mov_b32 s2, 0x41c00000
	v_cndmask_b32_e32 v74, v243, v74, vcc
	v_cmp_ne_u32_e32 vcc, 0, v78
	s_mov_b32 s3, 0x41c80000
	v_and_b32_e32 v81, 0x1000000, v83
	v_cndmask_b32_e32 v77, v243, v77, vcc
	v_cmp_ne_u32_e32 vcc, 0, v79
	v_pk_fma_f32 v[78:79], v[188:189], s[2:3], v[82:83] op_sel_hi:[1,1,0]
	s_mov_b32 s2, 0x41d00000
	v_cndmask_b32_e32 v76, v243, v76, vcc
	v_cmp_ne_u32_e32 vcc, 0, v80
	s_mov_b32 s3, 0x41d80000
	v_and_b32_e32 v84, 0x8000000, v83
	v_cndmask_b32_e32 v79, v243, v79, vcc
	v_cmp_ne_u32_e32 vcc, 0, v81
	v_lshrrev_b32_e32 v98, v208, v197
	v_pk_fma_f32 v[80:81], v[188:189], s[2:3], v[82:83] op_sel_hi:[1,1,0]
	v_cndmask_b32_e32 v78, v243, v78, vcc
	v_and_b32_e32 v83, 0x4000000, v83
	v_cmp_ne_u32_e32 vcc, 0, v84
	v_and_b32_e32 v99, 0x8000000, v98
	v_pk_fma_f32 v[96:97], v[188:189], s[68:69], v[82:83] op_sel_hi:[1,1,0]
	v_cndmask_b32_e32 v81, v243, v81, vcc
	v_cmp_ne_u32_e32 vcc, 0, v83
	v_pk_fma_f32 v[94:95], v[188:189], s[96:97], v[82:83] op_sel_hi:[1,1,0]
	v_pk_fma_f32 v[92:93], v[188:189], s[94:95], v[82:83] op_sel_hi:[1,1,0]
	v_cndmask_b32_e32 v80, v243, v80, vcc
	v_cmp_ne_u32_e32 vcc, 0, v99
	v_and_b32_e32 v99, 0x4000000, v98
	v_pk_fma_f32 v[90:91], v[188:189], s[92:93], v[82:83] op_sel_hi:[1,1,0]
	v_cndmask_b32_e32 v97, v243, v97, vcc
	v_cmp_ne_u32_e32 vcc, 0, v99
	v_and_b32_e32 v99, 0x2000000, v98
	v_pk_fma_f32 v[88:89], v[188:189], s[90:91], v[82:83] op_sel_hi:[1,1,0]
	v_cndmask_b32_e32 v96, v243, v96, vcc
	v_cmp_ne_u32_e32 vcc, 0, v99
	v_and_b32_e32 v99, 0x1000000, v98
	v_pk_fma_f32 v[86:87], v[188:189], s[88:89], v[82:83] op_sel_hi:[1,1,0]
	v_cndmask_b32_e32 v95, v243, v95, vcc
	v_cmp_ne_u32_e32 vcc, 0, v99
	v_and_b32_e32 v99, 0x80000, v98
	v_pk_fma_f32 v[84:85], v[188:189], s[86:87], v[82:83] op_sel_hi:[1,1,0]
	v_cndmask_b32_e32 v94, v243, v94, vcc
	v_cmp_ne_u32_e32 vcc, 0, v99
	v_and_b32_e32 v99, 0x40000, v98
	s_mov_b32 s2, 0x42000000
	v_cndmask_b32_e32 v93, v243, v93, vcc
	v_cmp_ne_u32_e32 vcc, 0, v99
	v_and_b32_e32 v99, 0x20000, v98
	s_mov_b32 s3, 0x42040000
	v_cndmask_b32_e32 v92, v243, v92, vcc
	v_cmp_ne_u32_e32 vcc, 0, v99
	v_and_b32_e32 v99, 0x10000, v98
	v_pk_fma_f32 v[82:83], v[184:185], s[2:3], v[82:83] op_sel_hi:[1,1,0]
	v_cndmask_b32_e32 v91, v243, v91, vcc
	v_cmp_ne_u32_e32 vcc, 0, v99
	v_and_b32_e32 v99, 0x800, v98
	s_nop 0
	v_cndmask_b32_e32 v90, v243, v90, vcc
	v_cmp_ne_u32_e32 vcc, 0, v99
	v_and_b32_e32 v99, 0x400, v98
	s_nop 0
	v_cndmask_b32_e32 v89, v243, v89, vcc
	v_cmp_ne_u32_e32 vcc, 0, v99
	v_and_b32_e32 v99, 0x200, v98
	s_nop 0
	v_cndmask_b32_e32 v88, v243, v88, vcc
	v_cmp_ne_u32_e32 vcc, 0, v99
	v_and_b32_e32 v99, 0x100, v98
	s_nop 0
	v_cndmask_b32_e32 v87, v243, v87, vcc
	v_cmp_ne_u32_e32 vcc, 0, v99
	v_and_b32_e32 v99, 8, v98
	s_nop 0
	v_cndmask_b32_e32 v86, v243, v86, vcc
	v_cmp_ne_u32_e32 vcc, 0, v99
	v_and_b32_e32 v99, 4, v98
	s_nop 0
	v_cndmask_b32_e32 v85, v243, v85, vcc
	v_cmp_ne_u32_e32 vcc, 0, v99
	v_and_b32_e32 v99, 2, v98
	v_and_b32_e32 v98, 1, v98
	v_cndmask_b32_e32 v84, v243, v84, vcc
	v_cmp_ne_u32_e32 vcc, 0, v99
	s_nop 1
	v_cndmask_b32_e32 v83, v243, v83, vcc
	v_cmp_eq_u32_e32 vcc, 1, v98
	s_nop 1
	v_cndmask_b32_e32 v82, v243, v82, vcc
	s_setprio 1
	ds_read_b128 v[114:117], v211 offset:49152
	ds_read_b128 v[124:127], v211 offset:57344
	s_waitcnt lgkmcnt(1)
	v_mfma_f32_32x32x16_bf16 v[66:81], v[114:117], v[158:161], v[66:81]
	ds_read_b128 v[114:117], v212 offset:49152
	s_waitcnt lgkmcnt(1)
	v_mfma_f32_32x32x16_bf16 v[82:97], v[124:127], v[158:161], v[82:97]
	ds_read_b128 v[124:127], v212 offset:57344
	s_waitcnt lgkmcnt(1)
	v_mfma_f32_32x32x16_bf16 v[66:81], v[114:117], v[154:157], v[66:81]
	ds_read_b128 v[114:117], v213 offset:49152
	s_waitcnt lgkmcnt(1)
	v_mfma_f32_32x32x16_bf16 v[82:97], v[124:127], v[154:157], v[82:97]
	ds_read_b128 v[124:127], v213 offset:57344
	s_waitcnt lgkmcnt(1)
	v_mfma_f32_32x32x16_bf16 v[66:81], v[114:117], v[150:153], v[66:81]
	ds_read_b128 v[114:117], v214 offset:49152
	s_waitcnt lgkmcnt(1)
	v_mfma_f32_32x32x16_bf16 v[82:97], v[124:127], v[150:153], v[82:97]
	ds_read_b128 v[124:127], v214 offset:57344
	s_waitcnt lgkmcnt(1)
	v_mfma_f32_32x32x16_bf16 v[66:81], v[114:117], v[146:149], v[66:81]
	ds_read_b128 v[114:117], v211 offset:49280
	s_waitcnt lgkmcnt(1)
	v_mfma_f32_32x32x16_bf16 v[82:97], v[124:127], v[146:149], v[82:97]
	ds_read_b128 v[124:127], v211 offset:57472
	s_waitcnt lgkmcnt(1)
	v_mfma_f32_32x32x16_bf16 v[66:81], v[114:117], v[142:145], v[66:81]
	ds_read_b128 v[114:117], v212 offset:49280
	s_waitcnt lgkmcnt(1)
	v_mfma_f32_32x32x16_bf16 v[82:97], v[124:127], v[142:145], v[82:97]
	ds_read_b128 v[124:127], v212 offset:57472
	s_waitcnt lgkmcnt(1)
	v_mfma_f32_32x32x16_bf16 v[66:81], v[114:117], v[138:141], v[66:81]
	ds_read_b128 v[114:117], v213 offset:49280
	s_waitcnt lgkmcnt(1)
	v_mfma_f32_32x32x16_bf16 v[82:97], v[124:127], v[138:141], v[82:97]
	ds_read_b128 v[124:127], v213 offset:57472
	s_waitcnt lgkmcnt(1)
	v_mfma_f32_32x32x16_bf16 v[66:81], v[114:117], v[134:137], v[66:81]
	ds_read_b128 v[114:117], v214 offset:49280
	s_waitcnt lgkmcnt(1)
	v_mfma_f32_32x32x16_bf16 v[82:97], v[124:127], v[134:137], v[82:97]
	ds_read_b128 v[124:127], v214 offset:57472
	s_waitcnt lgkmcnt(1)
	v_mfma_f32_32x32x16_bf16 v[66:81], v[114:117], v[130:133], v[66:81]
	s_waitcnt lgkmcnt(0)
	v_mfma_f32_32x32x16_bf16 v[82:97], v[124:127], v[130:133], v[82:97]
	s_setprio 0
	global_load_dwordx2 v[196:197], v[194:195], off
	v_readlane_b32 vcc_lo, v255, 63
	s_bitcmp1_b32 vcc_lo, 0
	s_cbranch_scc1 .Lsw1_done
.Lsw1_B:
	v_add_f32_e32 v98, 0, v225
	v_add_f32_e32 v98, v229, v98
	v_add_f32_e32 v98, v226, v98
	v_add_f32_e32 v98, v230, v98
	v_add_f32_e32 v98, v227, v98
	v_add_f32_e32 v98, v231, v98
	v_add_f32_e32 v98, v228, v98
	v_add_f32_e32 v98, v232, v98
	v_add_f32_e32 v98, v173, v98
	v_add_f32_e32 v98, v177, v98
	v_add_f32_e32 v98, v174, v98
	v_add_f32_e32 v98, v222, v98
	v_exp_f32_e32 v106, v170
	v_add_f32_e32 v98, v175, v98
	v_exp_f32_e32 v107, v171
	v_add_f32_e32 v98, v223, v98
	v_exp_f32_e32 v108, v168
	v_add_f32_e32 v98, v176, v98
	v_exp_f32_e32 v109, v169
	v_add_f32_e32 v98, v224, v98
	v_exp_f32_e32 v110, v166
	v_add_f32_e32 v98, v106, v98
	v_exp_f32_e32 v111, v167
	v_add_f32_e32 v98, v107, v98
	v_exp_f32_e32 v112, v164
	v_add_f32_e32 v98, v108, v98
	v_exp_f32_e32 v113, v165
	v_add_f32_e32 v98, v109, v98
	v_exp_f32_e32 v114, v162
	v_add_f32_e32 v98, v110, v98
	v_exp_f32_e32 v115, v163
	v_add_f32_e32 v98, v111, v98
	v_exp_f32_e32 v116, v122
	v_add_f32_e32 v98, v112, v98
	v_exp_f32_e32 v117, v123
	v_add_f32_e32 v98, v113, v98
	v_exp_f32_e32 v120, v120
	v_add_f32_e32 v98, v114, v98
	v_exp_f32_e32 v121, v121
	v_add_f32_e32 v98, v115, v98
	v_exp_f32_e32 v118, v118
	v_add_f32_e32 v98, v116, v98
	v_exp_f32_e32 v119, v119
	v_add_f32_e32 v98, v117, v98
	v_add_f32_e32 v98, v120, v98
	v_add_f32_e32 v98, v121, v98
	v_add_f32_e32 v98, v118, v98
	v_add_f32_e32 v219, v119, v98
	v_mov_b32_e32 v220, v219
	s_nop 1
	v_permlane32_swap_b32_e32 v219, v220
	v_cvt_pk_bf16_f32 v98, v225, v229
	v_cvt_pk_bf16_f32 v99, v226, v230
	v_cvt_pk_bf16_f32 v100, v227, v231
	v_cvt_pk_bf16_f32 v101, v228, v232
	v_cvt_pk_bf16_f32 v102, v173, v177
	v_cvt_pk_bf16_f32 v103, v174, v222
	v_cvt_pk_bf16_f32 v104, v175, v223
	v_cvt_pk_bf16_f32 v105, v176, v224
	v_cvt_pk_bf16_f32 v106, v106, v107
	v_cvt_pk_bf16_f32 v107, v108, v109
	v_cvt_pk_bf16_f32 v108, v110, v111
	v_cvt_pk_bf16_f32 v109, v112, v113
	v_cvt_pk_bf16_f32 v110, v114, v115
	v_cvt_pk_bf16_f32 v111, v116, v117
	v_cvt_pk_bf16_f32 v112, v120, v121
	v_cvt_pk_bf16_f32 v113, v118, v119
	s_nop 0
	v_permlane32_swap_b32_e32 v98, v100
	v_permlane32_swap_b32_e32 v99, v101
	v_permlane32_swap_b32_e32 v102, v104
	v_permlane32_swap_b32_e32 v103, v105
	v_permlane32_swap_b32_e32 v106, v108
	v_permlane32_swap_b32_e32 v107, v109
	v_permlane32_swap_b32_e32 v110, v112
	v_permlane32_swap_b32_e32 v111, v113
	v_readlane_b32 vcc_lo, v255, 63
	s_bitcmp1_b32 vcc_lo, 0
	s_cbranch_scc1 .Lsw1_A
.Lsw1_done:
	v_mad_i64_i32 v[114:115], s[2:3], v217, s84, v[190:191]
	v_add_u32_e32 v118, 32, v217
	v_mad_i64_i32 v[116:117], s[2:3], v118, s84, v[190:191]
	global_load_dwordx4 v[162:165], v[114:115], off
	global_load_dwordx4 v[166:169], v[116:117], off
	v_mad_i64_i32 v[114:115], s[2:3], v217, s84, v[192:193]
	v_mad_i64_i32 v[116:117], s[2:3], v118, s84, v[192:193]
	global_load_dwordx4 v[170:173], v[114:115], off
	global_load_dwordx4 v[174:177], v[116:117], off
	s_setprio 1
	ds_read_b64_tr_b16 v[114:115], v201 offset:0
	ds_read_b64_tr_b16 v[116:117], v201 offset:0x800
	ds_read_b64_tr_b16 v[118:119], v201 offset:0x1000
	ds_read_b64_tr_b16 v[120:121], v201 offset:0x1800
	ds_read_b64_tr_b16 v[122:123], v201 offset:0x2000
	ds_read_b64_tr_b16 v[124:125], v201 offset:0x2800
	ds_read_b64_tr_b16 v[126:127], v201 offset:0x3000
	ds_read_b64_tr_b16 v[128:129], v201 offset:0x3800
	s_waitcnt lgkmcnt(0)
	s_nop 0
	v_mfma_f32_32x32x16_bf16 v[2:17], v[98:101], v[114:117], v[2:17]
	ds_read_b64_tr_b16 v[114:115], v201 offset:0x200
	ds_read_b64_tr_b16 v[116:117], v201 offset:0xa00
	v_mfma_f32_32x32x16_bf16 v[2:17], v[102:105], v[118:121], v[2:17]
	ds_read_b64_tr_b16 v[118:119], v201 offset:0x1200
	ds_read_b64_tr_b16 v[120:121], v201 offset:0x1a00
	v_mfma_f32_32x32x16_bf16 v[2:17], v[106:109], v[122:125], v[2:17]
	ds_read_b64_tr_b16 v[122:123], v201 offset:0x2200
	ds_read_b64_tr_b16 v[124:125], v201 offset:0x2a00
	v_mfma_f32_32x32x16_bf16 v[2:17], v[110:113], v[126:129], v[2:17]
	ds_read_b64_tr_b16 v[126:127], v201 offset:0x3200
	ds_read_b64_tr_b16 v[128:129], v201 offset:0x3a00
	s_waitcnt lgkmcnt(0)
	v_mfma_f32_32x32x16_bf16 v[50:65], v[98:101], v[114:117], v[50:65]
	ds_read_b64_tr_b16 v[114:115], v201 offset:0x400
	ds_read_b64_tr_b16 v[116:117], v201 offset:0xc00
	v_mfma_f32_32x32x16_bf16 v[50:65], v[102:105], v[118:121], v[50:65]
	ds_read_b64_tr_b16 v[118:119], v201 offset:0x1400
	ds_read_b64_tr_b16 v[120:121], v201 offset:0x1c00
	v_mfma_f32_32x32x16_bf16 v[50:65], v[106:109], v[122:125], v[50:65]
	ds_read_b64_tr_b16 v[122:123], v201 offset:0x2400
	ds_read_b64_tr_b16 v[124:125], v201 offset:0x2c00
	v_mfma_f32_32x32x16_bf16 v[50:65], v[110:113], v[126:129], v[50:65]
	ds_read_b64_tr_b16 v[126:127], v201 offset:0x3400
	ds_read_b64_tr_b16 v[128:129], v201 offset:0x3c00
	s_waitcnt lgkmcnt(0)
	v_mfma_f32_32x32x16_bf16 v[34:49], v[98:101], v[114:117], v[34:49]
	ds_read_b64_tr_b16 v[114:115], v201 offset:0x600
	ds_read_b64_tr_b16 v[116:117], v201 offset:0xe00
	v_mfma_f32_32x32x16_bf16 v[34:49], v[102:105], v[118:121], v[34:49]
	ds_read_b64_tr_b16 v[118:119], v201 offset:0x1600
	ds_read_b64_tr_b16 v[120:121], v201 offset:0x1e00
	v_mfma_f32_32x32x16_bf16 v[34:49], v[106:109], v[122:125], v[34:49]
	ds_read_b64_tr_b16 v[122:123], v201 offset:0x2600
	ds_read_b64_tr_b16 v[124:125], v201 offset:0x2e00
	v_mfma_f32_32x32x16_bf16 v[34:49], v[110:113], v[126:129], v[34:49]
	ds_read_b64_tr_b16 v[126:127], v201 offset:0x3600
	ds_read_b64_tr_b16 v[128:129], v201 offset:0x3e00
	s_waitcnt lgkmcnt(0)
	v_mfma_f32_32x32x16_bf16 v[18:33], v[98:101], v[114:117], v[18:33]
	v_mfma_f32_32x32x16_bf16 v[18:33], v[102:105], v[118:121], v[18:33]
	v_mfma_f32_32x32x16_bf16 v[18:33], v[106:109], v[122:125], v[18:33]
	v_mfma_f32_32x32x16_bf16 v[18:33], v[110:113], v[126:129], v[18:33]
	s_setprio 0
	v_max_f32_e32 v98, v67, v67
	v_max_f32_e32 v99, v66, v66
	v_max_f32_e32 v98, v99, v98
	v_max3_f32 v98, v98, v68, v69
	v_max3_f32 v98, v98, v70, v71
	v_max3_f32 v98, v98, v72, v73
	v_max3_f32 v98, v98, v74, v75
	v_max3_f32 v98, v98, v76, v77
	v_max3_f32 v98, v98, v78, v79
	v_max3_f32 v98, v98, v80, v81
	v_max3_f32 v98, v98, v82, v83
	v_max3_f32 v98, v98, v84, v85
	v_max3_f32 v98, v98, v86, v87
	v_max3_f32 v98, v98, v88, v89
	v_max3_f32 v98, v98, v90, v91
	v_max3_f32 v98, v98, v92, v93
	v_max3_f32 v98, v98, v94, v95
	v_max3_f32 v98, v98, v96, v97
	v_mov_b32_e32 v99, v98
	s_nop 1
	v_permlane32_swap_b32_e32 v98, v99
	v_max_f32_e32 v99, v99, v99
	v_max_f32_e32 v98, v98, v98
	v_max_f32_e32 v98, v98, v99
	v_sub_f32_e32 v99, v98, v215
	v_mul_f32_e32 v99, 0x3db504f3, v99
	v_cmp_ge_f32_e32 vcc, s74, v99
	v_max_f32_e32 v99, v215, v215
	v_max_f32_e32 v222, v99, v98
	v_sub_f32_e32 v98, v215, v222
	v_mul_f32_e32 v98, 0x3e0293ee, v98
	v_exp_f32_e32 v98, v98
	s_cmp_eq_u64 vcc, exec
	s_waitcnt lgkmcnt(0)
	s_barrier
	s_cselect_b64 s[2:3], -1, 0
	s_waitcnt vmcnt(0)
	v_cndmask_b32_e64 v221, v98, 1.0, s[2:3]
	v_cmp_gt_f32_e32 vcc, 1.0, v221
	s_waitcnt vmcnt(3)
	ds_write_b128 v210, v[162:165]
	s_waitcnt vmcnt(2)
	ds_write_b128 v210, v[166:169] offset:8192
	s_waitcnt vmcnt(1)
	ds_write_b128 v204, v[170:173] offset:32768
	s_waitcnt vmcnt(0)
	ds_write_b128 v204, v[174:177] offset:40960
	s_cbranch_vccz .LBB0_1147
	s_and_saveexec_b64 s[4:5], s[0:1]
	ds_write_b32 v206, v221 offset:128
	s_or_b64 exec, exec, s[4:5]
	s_waitcnt lgkmcnt(0)
	ds_read_b128 v[98:101], v205 offset:224
	ds_read_b128 v[102:105], v205 offset:192
	ds_read_b128 v[106:109], v205 offset:160
	ds_read_b128 v[110:113], v205 offset:128
	v_readlane_b32 s56, v254, 33
	s_waitcnt lgkmcnt(3)
	v_pk_mul_f32 v[16:17], v[16:17], v[100:101]
	s_waitcnt lgkmcnt(2)
	v_pk_mul_f32 v[12:13], v[12:13], v[104:105]
	s_waitcnt lgkmcnt(1)
	v_pk_mul_f32 v[8:9], v[8:9], v[108:109]
	s_waitcnt lgkmcnt(0)
	v_pk_mul_f32 v[4:5], v[4:5], v[112:113]
	v_pk_mul_f32 v[14:15], v[14:15], v[98:99]
	v_pk_mul_f32 v[10:11], v[10:11], v[102:103]
	v_pk_mul_f32 v[6:7], v[6:7], v[106:107]
	v_pk_mul_f32 v[2:3], v[2:3], v[110:111]
	v_pk_mul_f32 v[64:65], v[64:65], v[100:101]
	v_pk_mul_f32 v[60:61], v[60:61], v[104:105]
	v_pk_mul_f32 v[56:57], v[56:57], v[108:109]
	v_pk_mul_f32 v[52:53], v[52:53], v[112:113]
	v_pk_mul_f32 v[62:63], v[62:63], v[98:99]
	v_pk_mul_f32 v[58:59], v[58:59], v[102:103]
	v_pk_mul_f32 v[54:55], v[54:55], v[106:107]
	v_pk_mul_f32 v[50:51], v[50:51], v[110:111]
	v_pk_mul_f32 v[48:49], v[48:49], v[100:101]
	v_pk_mul_f32 v[44:45], v[44:45], v[104:105]
	v_pk_mul_f32 v[40:41], v[40:41], v[108:109]
	v_pk_mul_f32 v[36:37], v[36:37], v[112:113]
	v_pk_mul_f32 v[46:47], v[46:47], v[98:99]
	v_pk_mul_f32 v[42:43], v[42:43], v[102:103]
	v_pk_mul_f32 v[38:39], v[38:39], v[106:107]
	v_pk_mul_f32 v[34:35], v[34:35], v[110:111]
	v_pk_mul_f32 v[32:33], v[32:33], v[100:101]
	v_pk_mul_f32 v[28:29], v[28:29], v[104:105]
	v_pk_mul_f32 v[24:25], v[24:25], v[108:109]
	v_pk_mul_f32 v[20:21], v[20:21], v[112:113]
	v_pk_mul_f32 v[30:31], v[30:31], v[98:99]
	v_pk_mul_f32 v[26:27], v[26:27], v[102:103]
	v_pk_mul_f32 v[22:23], v[22:23], v[106:107]
	v_pk_mul_f32 v[18:19], v[18:19], v[110:111]
	v_readlane_b32 s57, v254, 34

.Lsw0_A:
	v_add_u32_e32 v146, 64, v199
	v_cvt_f32_i32_e32 v66, v146
	s_sub_i32 s2, s85, 63
	s_lshr_b32 s2, s2, 8
	v_lshrrev_b32_sdwa v67, s2, v192 dst_sel:DWORD dst_unused:UNUSED_PAD src0_sel:DWORD src1_sel:WORD_0
	v_and_b32_e32 v67, 1, v67
	v_mul_f32_e64 v66, -v162, v66
	v_cmp_eq_u32_e32 vcc, 1, v67
	s_mov_b32 s2, 0x41900000
	s_mov_b32 s3, 0x41980000
	v_cndmask_b32_e32 v82, v243, v66, vcc
	v_pk_fma_f32 v[76:77], v[170:171], s[2:3], v[82:83] op_sel_hi:[1,1,0]
	s_mov_b32 s2, 0x41c00000
	s_mov_b32 s3, 0x41c80000
	v_pk_fma_f32 v[78:79], v[170:171], s[2:3], v[82:83] op_sel_hi:[1,1,0]
	s_mov_b32 s2, 0x41d00000
	s_mov_b32 s3, 0x41d80000
	v_pk_fma_f32 v[80:81], v[170:171], s[2:3], v[82:83] op_sel_hi:[1,1,0]
	s_mov_b32 s2, 0x42000000
	s_mov_b32 s3, 0x42040000
	v_fma_f32 v66, 0, v162, v82
	v_add_f32_e32 v67, v162, v82
	v_pk_fma_f32 v[68:69], v[170:171], s[60:61], v[82:83] op_sel_hi:[1,1,0]
	v_pk_fma_f32 v[70:71], v[170:171], s[74:75], v[82:83] op_sel_hi:[1,1,0]
	v_pk_fma_f32 v[72:73], v[170:171], s[62:63], v[82:83] op_sel_hi:[1,1,0]
	v_pk_fma_f32 v[74:75], v[170:171], s[58:59], v[82:83] op_sel_hi:[1,1,0]
	v_pk_fma_f32 v[96:97], v[170:171], s[68:69], v[82:83] op_sel_hi:[1,1,0]
	v_pk_fma_f32 v[94:95], v[170:171], s[96:97], v[82:83] op_sel_hi:[1,1,0]
	v_pk_fma_f32 v[92:93], v[170:171], s[94:95], v[82:83] op_sel_hi:[1,1,0]
	v_pk_fma_f32 v[90:91], v[170:171], s[92:93], v[82:83] op_sel_hi:[1,1,0]
	v_pk_fma_f32 v[88:89], v[170:171], s[90:91], v[82:83] op_sel_hi:[1,1,0]
	v_pk_fma_f32 v[86:87], v[170:171], s[88:89], v[82:83] op_sel_hi:[1,1,0]
	v_pk_fma_f32 v[84:85], v[170:171], s[86:87], v[82:83] op_sel_hi:[1,1,0]
	v_pk_fma_f32 v[82:83], v[168:169], s[2:3], v[82:83] op_sel_hi:[1,1,0]
	s_setprio 1
	ds_read_b128 v[130:133], v195 offset:49152
	ds_read_b128 v[134:137], v195 offset:57344
	ds_read_b128 v[138:141], v196 offset:49152
	ds_read_b128 v[142:145], v196 offset:57344
	s_waitcnt lgkmcnt(3)
	v_mfma_f32_32x32x16_bf16 v[66:81], v[130:133], v[126:129], v[66:81]
	ds_read_b128 v[130:133], v197 offset:49152
	s_waitcnt lgkmcnt(3)
	v_mfma_f32_32x32x16_bf16 v[82:97], v[134:137], v[126:129], v[82:97]
	ds_read_b128 v[134:137], v197 offset:57344
	s_waitcnt lgkmcnt(3)
	v_mfma_f32_32x32x16_bf16 v[66:81], v[138:141], v[122:125], v[66:81]
	ds_read_b128 v[138:141], v198 offset:49152
	s_waitcnt lgkmcnt(3)
	v_mfma_f32_32x32x16_bf16 v[82:97], v[142:145], v[122:125], v[82:97]
	ds_read_b128 v[142:145], v198 offset:57344
	s_waitcnt lgkmcnt(3)
	v_mfma_f32_32x32x16_bf16 v[66:81], v[130:133], v[118:121], v[66:81]
	ds_read_b128 v[130:133], v195 offset:49280
	s_waitcnt lgkmcnt(3)
	v_mfma_f32_32x32x16_bf16 v[82:97], v[134:137], v[118:121], v[82:97]
	ds_read_b128 v[134:137], v195 offset:57472
	s_waitcnt lgkmcnt(3)
	v_mfma_f32_32x32x16_bf16 v[66:81], v[138:141], v[114:117], v[66:81]
	ds_read_b128 v[138:141], v196 offset:49280
	s_waitcnt lgkmcnt(3)
	v_mfma_f32_32x32x16_bf16 v[82:97], v[142:145], v[114:117], v[82:97]
	ds_read_b128 v[142:145], v196 offset:57472
	s_waitcnt lgkmcnt(3)
	v_mfma_f32_32x32x16_bf16 v[66:81], v[130:133], v[110:113], v[66:81]
	ds_read_b128 v[130:133], v197 offset:49280
	s_waitcnt lgkmcnt(3)
	v_mfma_f32_32x32x16_bf16 v[82:97], v[134:137], v[110:113], v[82:97]
	ds_read_b128 v[134:137], v197 offset:57472
	s_waitcnt lgkmcnt(3)
	v_mfma_f32_32x32x16_bf16 v[66:81], v[138:141], v[106:109], v[66:81]
	ds_read_b128 v[138:141], v198 offset:49280
	s_waitcnt lgkmcnt(3)
	v_mfma_f32_32x32x16_bf16 v[82:97], v[142:145], v[106:109], v[82:97]
	ds_read_b128 v[142:145], v198 offset:57472
	s_waitcnt lgkmcnt(3)
	v_mfma_f32_32x32x16_bf16 v[66:81], v[130:133], v[102:105], v[66:81]
	s_waitcnt lgkmcnt(2)
	v_mfma_f32_32x32x16_bf16 v[82:97], v[134:137], v[102:105], v[82:97]
	s_waitcnt lgkmcnt(1)
	v_mfma_f32_32x32x16_bf16 v[66:81], v[138:141], v[98:101], v[66:81]
	s_waitcnt lgkmcnt(0)
	v_mfma_f32_32x32x16_bf16 v[82:97], v[142:145], v[98:101], v[82:97]
	s_setprio 0
	v_readlane_b32 vcc_lo, v255, 63
	s_bitcmp1_b32 vcc_lo, 0
	s_cbranch_scc1 .Lsw0_done
.Lsw0_B:
	v_add_f32_e32 v147, 0, v216
	v_add_f32_e32 v147, v220, v147
	v_add_f32_e32 v147, v217, v147
	v_add_f32_e32 v147, v221, v147
	v_add_f32_e32 v147, v218, v147
	v_add_f32_e32 v147, v222, v147
	v_add_f32_e32 v147, v219, v147
	v_add_f32_e32 v147, v223, v147
	v_add_f32_e32 v147, v208, v147
	v_add_f32_e32 v147, v212, v147
	v_add_f32_e32 v147, v209, v147
	v_add_f32_e32 v147, v213, v147
	v_exp_f32_e32 v130, v178
	v_add_f32_e32 v147, v210, v147
	v_exp_f32_e32 v131, v179
	v_add_f32_e32 v147, v214, v147
	v_exp_f32_e32 v132, v176
	v_add_f32_e32 v147, v211, v147
	v_exp_f32_e32 v133, v177
	v_add_f32_e32 v147, v215, v147
	s_waitcnt vmcnt(2)
	v_exp_f32_e32 v134, v160
	v_add_f32_e32 v147, v130, v147
	v_exp_f32_e32 v135, v161
	v_add_f32_e32 v147, v131, v147
	v_exp_f32_e32 v136, v158
	v_add_f32_e32 v147, v132, v147
	v_exp_f32_e32 v137, v159
	v_add_f32_e32 v147, v133, v147
	s_waitcnt vmcnt(1)
	v_exp_f32_e32 v138, v156
	v_add_f32_e32 v147, v134, v147
	v_exp_f32_e32 v139, v157
	v_add_f32_e32 v147, v135, v147
	v_exp_f32_e32 v140, v154
	v_add_f32_e32 v147, v136, v147
	v_exp_f32_e32 v141, v155
	v_add_f32_e32 v147, v137, v147
	s_waitcnt vmcnt(0)
	v_exp_f32_e32 v142, v152
	v_add_f32_e32 v147, v138, v147
	v_exp_f32_e32 v143, v153
	v_add_f32_e32 v147, v139, v147
	v_exp_f32_e32 v144, v150
	v_add_f32_e32 v147, v140, v147
	v_exp_f32_e32 v145, v151
	v_add_f32_e32 v147, v141, v147
	v_add_f32_e32 v147, v142, v147
	v_add_f32_e32 v147, v143, v147
	v_add_f32_e32 v147, v144, v147
	v_add_f32_e32 v204, v145, v147
	v_mov_b32_e32 v205, v204
	s_nop 1
	v_permlane32_swap_b32_e32 v204, v205
	v_cvt_pk_bf16_f32 v148, v216, v220
	v_cvt_pk_bf16_f32 v149, v217, v221
	v_cvt_pk_bf16_f32 v150, v218, v222
	v_cvt_pk_bf16_f32 v151, v219, v223
	v_cvt_pk_bf16_f32 v152, v208, v212
	v_cvt_pk_bf16_f32 v153, v209, v213
	v_cvt_pk_bf16_f32 v154, v210, v214
	v_cvt_pk_bf16_f32 v155, v211, v215
	v_cvt_pk_bf16_f32 v156, v130, v131
	v_cvt_pk_bf16_f32 v157, v132, v133
	v_cvt_pk_bf16_f32 v158, v134, v135
	v_cvt_pk_bf16_f32 v159, v136, v137
	v_cvt_pk_bf16_f32 v206, v138, v139
	v_cvt_pk_bf16_f32 v207, v140, v141
	v_cvt_pk_bf16_f32 v208, v142, v143
	v_cvt_pk_bf16_f32 v209, v144, v145
	s_nop 0
	v_permlane32_swap_b32_e32 v148, v150
	v_permlane32_swap_b32_e32 v149, v151
	v_permlane32_swap_b32_e32 v152, v154
	v_permlane32_swap_b32_e32 v153, v155
	v_permlane32_swap_b32_e32 v156, v158
	v_permlane32_swap_b32_e32 v157, v159
	v_permlane32_swap_b32_e32 v206, v208
	v_permlane32_swap_b32_e32 v207, v209
	v_readlane_b32 vcc_lo, v255, 63
	s_bitcmp1_b32 vcc_lo, 0
	s_cbranch_scc1 .Lsw0_A
.Lsw0_done:
	v_add_u32_e32 v177, s85, v167
	v_add_u32_e32 v138, 1, v177
	v_add_u32_e32 v140, 33, v177
	v_mad_i64_i32 v[130:131], s[2:3], v138, s71, v[172:173]
	v_mad_i64_i32 v[134:135], s[2:3], v140, s71, v[172:173]
	v_mad_i64_i32 v[138:139], s[2:3], v138, s71, v[174:175]
	v_mad_i64_i32 v[142:143], s[2:3], v140, s71, v[174:175]
	global_load_dwordx4 v[130:133], v[130:131], off
	s_nop 0
	global_load_dwordx4 v[134:137], v[134:135], off
	s_nop 0
	global_load_dwordx4 v[138:141], v[138:139], off
	s_nop 0
	global_load_dwordx4 v[142:145], v[142:143], off
	s_setprio 1
	ds_read_b64_tr_b16 v[210:211], v188 offset:0
	ds_read_b64_tr_b16 v[212:213], v188 offset:0x800
	ds_read_b64_tr_b16 v[214:215], v188 offset:0x1000
	ds_read_b64_tr_b16 v[216:217], v188 offset:0x1800
	ds_read_b64_tr_b16 v[218:219], v188 offset:0x2000
	ds_read_b64_tr_b16 v[220:221], v188 offset:0x2800
	ds_read_b64_tr_b16 v[222:223], v188 offset:0x3000
	ds_read_b64_tr_b16 v[224:225], v188 offset:0x3800
	s_waitcnt lgkmcnt(0)
	s_nop 0
	v_mfma_f32_32x32x16_bf16 v[34:49], v[148:151], v[210:213], v[34:49]
	ds_read_b64_tr_b16 v[210:211], v188 offset:0x200
	ds_read_b64_tr_b16 v[212:213], v188 offset:0xa00
	v_mfma_f32_32x32x16_bf16 v[34:49], v[152:155], v[214:217], v[34:49]
	ds_read_b64_tr_b16 v[214:215], v188 offset:0x1200
	ds_read_b64_tr_b16 v[216:217], v188 offset:0x1a00
	v_mfma_f32_32x32x16_bf16 v[34:49], v[156:159], v[218:221], v[34:49]
	ds_read_b64_tr_b16 v[218:219], v188 offset:0x2200
	ds_read_b64_tr_b16 v[220:221], v188 offset:0x2a00
	v_mfma_f32_32x32x16_bf16 v[34:49], v[206:209], v[222:225], v[34:49]
	ds_read_b64_tr_b16 v[222:223], v188 offset:0x3200
	ds_read_b64_tr_b16 v[224:225], v188 offset:0x3a00
	s_waitcnt lgkmcnt(0)
	v_mfma_f32_32x32x16_bf16 v[50:65], v[148:151], v[210:213], v[50:65]
	ds_read_b64_tr_b16 v[210:211], v188 offset:0x400
	ds_read_b64_tr_b16 v[212:213], v188 offset:0xc00
	v_mfma_f32_32x32x16_bf16 v[50:65], v[152:155], v[214:217], v[50:65]
	ds_read_b64_tr_b16 v[214:215], v188 offset:0x1400
	ds_read_b64_tr_b16 v[216:217], v188 offset:0x1c00
	v_mfma_f32_32x32x16_bf16 v[50:65], v[156:159], v[218:221], v[50:65]
	ds_read_b64_tr_b16 v[218:219], v188 offset:0x2400
	ds_read_b64_tr_b16 v[220:221], v188 offset:0x2c00
	v_mfma_f32_32x32x16_bf16 v[50:65], v[206:209], v[222:225], v[50:65]
	ds_read_b64_tr_b16 v[222:223], v188 offset:0x3400
	ds_read_b64_tr_b16 v[224:225], v188 offset:0x3c00
	s_waitcnt lgkmcnt(0)
	v_mfma_f32_32x32x16_bf16 v[18:33], v[148:151], v[210:213], v[18:33]
	ds_read_b64_tr_b16 v[210:211], v188 offset:0x600
	ds_read_b64_tr_b16 v[212:213], v188 offset:0xe00
	v_mfma_f32_32x32x16_bf16 v[18:33], v[152:155], v[214:217], v[18:33]
	ds_read_b64_tr_b16 v[214:215], v188 offset:0x1600
	ds_read_b64_tr_b16 v[216:217], v188 offset:0x1e00
	v_mfma_f32_32x32x16_bf16 v[18:33], v[156:159], v[218:221], v[18:33]
	ds_read_b64_tr_b16 v[218:219], v188 offset:0x2600
	ds_read_b64_tr_b16 v[220:221], v188 offset:0x2e00
	v_mfma_f32_32x32x16_bf16 v[18:33], v[206:209], v[222:225], v[18:33]
	ds_read_b64_tr_b16 v[222:223], v188 offset:0x3600
	ds_read_b64_tr_b16 v[224:225], v188 offset:0x3e00
	s_waitcnt lgkmcnt(0)
	v_mfma_f32_32x32x16_bf16 v[2:17], v[148:151], v[210:213], v[2:17]
	v_mfma_f32_32x32x16_bf16 v[2:17], v[152:155], v[214:217], v[2:17]
	v_mfma_f32_32x32x16_bf16 v[2:17], v[156:159], v[218:221], v[2:17]
	v_mfma_f32_32x32x16_bf16 v[2:17], v[206:209], v[222:225], v[2:17]
	s_setprio 0
	s_cmp_le_i32 s85, s78
	s_cbranch_scc1 .LBB0_1262
	v_cmp_gt_i32_e64 s[60:61], 26, v146
	v_cmp_gt_i32_e64 s[62:63], 27, v146
	v_cmp_gt_i32_e64 s[58:59], 25, v146
	s_and_b64 s[60:61], s[62:63], s[60:61]
	v_cmp_gt_i32_e64 s[56:57], 24, v146
	s_and_b64 s[58:59], s[60:61], s[58:59]
	v_cmp_gt_i32_e64 s[54:55], 19, v146
	s_and_b64 s[56:57], s[58:59], s[56:57]
	v_cmp_gt_i32_e64 s[52:53], 18, v146
	s_and_b64 s[54:55], s[56:57], s[54:55]
	v_cmp_gt_i32_e64 s[50:51], 17, v146
	s_and_b64 s[52:53], s[54:55], s[52:53]
	v_cmp_gt_i32_e64 s[48:49], 16, v146
	s_and_b64 s[50:51], s[52:53], s[50:51]
	v_cmp_gt_i32_e64 s[46:47], 11, v146
	s_and_b64 s[48:49], s[50:51], s[48:49]
	v_cmp_gt_i32_e64 s[44:45], 10, v146
	s_and_b64 s[46:47], s[48:49], s[46:47]
	v_cmp_gt_i32_e64 s[42:43], 9, v146
	s_and_b64 s[44:45], s[46:47], s[44:45]
	v_cmp_gt_i32_e64 s[40:41], 8, v146
	s_and_b64 s[42:43], s[44:45], s[42:43]
	v_cmp_gt_i32_e64 s[38:39], 3, v146
	s_and_b64 s[40:41], s[42:43], s[40:41]
	v_cmp_gt_i32_e64 s[36:37], 2, v146
	s_and_b64 s[38:39], s[40:41], s[38:39]
	v_cmp_gt_i32_e64 s[34:35], 1, v146
	s_and_b64 s[36:37], s[38:39], s[36:37]
	v_cmp_gt_i32_e64 s[30:31], 0, v146
	s_and_b64 s[34:35], s[36:37], s[34:35]
	s_and_b64 s[30:31], s[34:35], s[30:31]
	v_cmp_gt_i32_e64 s[28:29], 58, v146
	v_cndmask_b32_e64 v66, v66, v243, s[30:31]
	v_cmp_gt_i32_e64 s[30:31], 59, v146
	v_cmp_gt_i32_e64 s[26:27], 57, v146
	s_and_b64 s[28:29], s[30:31], s[28:29]
	v_cmp_gt_i32_e64 s[24:25], 56, v146
	s_and_b64 s[26:27], s[28:29], s[26:27]
	v_cmp_gt_i32_e64 s[22:23], 51, v146
	s_and_b64 s[24:25], s[26:27], s[24:25]
	v_cmp_gt_i32_e64 s[20:21], 50, v146
	s_and_b64 s[22:23], s[24:25], s[22:23]
	v_cmp_gt_i32_e64 s[18:19], 49, v146
	s_and_b64 s[20:21], s[22:23], s[20:21]
	v_cmp_gt_i32_e64 s[16:17], 48, v146
	s_and_b64 s[18:19], s[20:21], s[18:19]
	v_cmp_gt_i32_e64 s[14:15], 43, v146
	s_and_b64 s[16:17], s[18:19], s[16:17]
	v_cmp_gt_i32_e64 s[12:13], 42, v146
	s_and_b64 s[14:15], s[16:17], s[14:15]
	v_cmp_gt_i32_e64 s[10:11], 41, v146
	s_and_b64 s[12:13], s[14:15], s[12:13]
	v_cmp_gt_i32_e64 s[8:9], 40, v146
	s_and_b64 s[10:11], s[12:13], s[10:11]
	v_cmp_gt_i32_e64 s[6:7], 35, v146
	s_and_b64 s[8:9], s[10:11], s[8:9]
	v_cmp_gt_i32_e64 s[4:5], 34, v146
	s_and_b64 s[6:7], s[8:9], s[6:7]
	v_cmp_gt_i32_e64 s[2:3], 33, v146
	s_and_b64 s[4:5], s[6:7], s[4:5]
	v_cmp_gt_i32_e32 vcc, 32, v146
	s_and_b64 s[2:3], s[4:5], s[2:3]
	v_cndmask_b32_e64 v81, v81, v243, s[62:63]
	s_mov_b32 s62, 0x41200000
	v_cndmask_b32_e64 v80, v80, v243, s[60:61]
	s_mov_b32 s60, 2.0
	v_cndmask_b32_e64 v79, v79, v243, s[58:59]
	s_mov_b32 s58, 0x41800000
	s_and_b64 vcc, s[2:3], vcc
	s_mov_b32 s63, 0x41300000
	s_mov_b32 s61, 0x40400000
	s_mov_b32 s59, 0x41880000
	v_cndmask_b32_e64 v78, v78, v243, s[56:57]
	v_cndmask_b32_e64 v77, v77, v243, s[54:55]
	v_cndmask_b32_e64 v76, v76, v243, s[52:53]
	v_cndmask_b32_e64 v75, v75, v243, s[50:51]
	v_cndmask_b32_e64 v74, v74, v243, s[48:49]
	v_cndmask_b32_e64 v73, v73, v243, s[46:47]
	v_cndmask_b32_e64 v72, v72, v243, s[44:45]
	v_cndmask_b32_e64 v71, v71, v243, s[42:43]
	v_cndmask_b32_e64 v70, v70, v243, s[40:41]
	v_cndmask_b32_e64 v69, v69, v243, s[38:39]
	v_cndmask_b32_e64 v68, v68, v243, s[36:37]
	v_cndmask_b32_e64 v67, v67, v243, s[34:35]
	v_cndmask_b32_e64 v97, v97, v243, s[30:31]
	v_cndmask_b32_e64 v96, v96, v243, s[28:29]
	v_cndmask_b32_e64 v95, v95, v243, s[26:27]
	v_cndmask_b32_e64 v94, v94, v243, s[24:25]
	v_cndmask_b32_e64 v93, v93, v243, s[22:23]
	v_cndmask_b32_e64 v92, v92, v243, s[20:21]
	v_cndmask_b32_e64 v91, v91, v243, s[18:19]
	v_cndmask_b32_e64 v90, v90, v243, s[16:17]
	v_cndmask_b32_e64 v89, v89, v243, s[14:15]
	v_cndmask_b32_e64 v88, v88, v243, s[12:13]
	v_cndmask_b32_e64 v87, v87, v243, s[10:11]
	v_cndmask_b32_e64 v86, v86, v243, s[8:9]
	v_cndmask_b32_e64 v85, v85, v243, s[6:7]
	v_cndmask_b32_e64 v84, v84, v243, s[4:5]
	v_cndmask_b32_e64 v83, v83, v243, s[2:3]
	v_cndmask_b32_e32 v82, v82, v243, vcc
